# cache-policy hint: residual-stream loads in the out epilogue (last use of x) marked non-temporal
# speedup vs baseline: 1.0086x; 1.0086x over previous
; __device__ __forceinline__ int tid_opaque() { int t = threadIdx.x; asm volatile("" : "+v"(t)); return t; }
; __device__ __forceinline__ void phase_out(const Ptrs& p, LAS unsigned char* lds) {
;     ...
;         const int tid = tid_opaque(), wid = tid >> 6, lane = tid & 63, wr = wid >> 2, wc = wid & 3, fr = lane & 15, fq = lane >> 4;
;         const float* gm = mod + (size_t)(row0 / S) * NMOD + 2 * D;
; #pragma unroll
;         for (int ai = 0; ai < 2; ++ai)
; #pragma unroll
;             for (int m = 0; m < 4; ++m) { const int row = row0 + ai * 128 + wr * 64 + m * 16 + fr;
; #pragma unroll
;                 for (int bj = 0; bj < 2; ++bj)
; #pragma unroll
;                     for (int n = 0; n < 2; ++n) { const int c = col0 + bj * 128 + wc * 32 + n * 16 + fq * 4; const size_t o = (size_t)row * D + c;
;                         *(f32x4*)(x1 + o) = *(const f32x4*)(p.x + o) + *(const f32x4*)(gm + c) * acc[ai][bj][m][n]; } }
.LBB0_838:
	v_mov_b32_e32 v131, v0
	s_lshr_b32 s0, s35, 20
	v_ashrrev_i32_e32 v130, 2, v131
	s_add_i32 s0, s34, s0
	v_and_b32_e32 v130, 0xffffffc0, v130
	v_and_or_b32 v132, v131, 15, s34
	s_ashr_i32 s0, s0, 12
	v_add_u32_e32 v130, v132, v130
	v_lshrrev_b32_e32 v132, 1, v131
	v_lshrrev_b32_e32 v131, 2, v131
	s_mul_hi_i32 s28, s0, 0xc000
	s_mul_i32 s0, s0, 0xc000
	v_and_b32_e32 v132, 0x60, v132
	v_and_b32_e32 v131, 12, v131
	s_add_u32 s0, s30, s0
	v_or3_b32 v132, v131, v132, s67
	v_ashrrev_i32_e32 v131, 31, v130
	s_addc_u32 s28, s31, s28
	v_lshlrev_b64 v[144:145], 11, v[130:131]
	s_add_u32 s54, s0, 0x14000
	v_or_b32_e32 v134, v144, v132
	v_mov_b32_e32 v135, v145
	s_addc_u32 s55, s28, 0
	v_lshlrev_b64 v[146:147], 2, v[134:135]
	v_lshlrev_b32_e32 v133, 2, v132
	v_lshl_add_u64 v[148:149], s[52:53], 0, v[146:147]
	global_load_dwordx4 v[136:139], v133, s[54:55]
	global_load_dwordx4 v[140:143], v[148:149], off nt
	v_lshl_add_u64 v[146:147], s[40:41], 0, v[146:147]
	v_or_b32_e32 v131, 16, v132
	v_lshlrev_b32_e32 v134, 2, v131
	s_andn2_b64 vcc, exec, s[38:39]
	s_add_i32 s18, s18, s19
	s_waitcnt vmcnt(0)
	v_pk_fma_f32 v[128:129], v[128:129], v[138:139], v[142:143]
	v_pk_fma_f32 v[126:127], v[126:127], v[136:137], v[140:141]
	global_store_dwordx4 v[146:147], v[126:129], off
	global_load_dwordx4 v[136:139], v[148:149], off offset:64 nt
	global_load_dwordx4 v[140:143], v134, s[54:55]
	v_or_b32_e32 v128, v144, v131
	v_mov_b32_e32 v129, v145
	v_lshl_add_u64 v[128:129], v[128:129], 2, s[40:41]
	v_or_b32_e32 v126, 0x80, v132
	v_lshlrev_b32_e32 v127, 2, v126
	s_waitcnt vmcnt(0)
	v_pk_fma_f32 v[124:125], v[124:125], v[142:143], v[138:139]
	v_pk_fma_f32 v[122:123], v[122:123], v[140:141], v[136:137]
	global_store_dwordx4 v[128:129], v[122:125], off
	global_load_dwordx4 v[136:139], v[148:149], off offset:512 nt
	global_load_dwordx4 v[140:143], v127, s[54:55]
	v_or_b32_e32 v124, v144, v126
	v_mov_b32_e32 v125, v145
	v_lshl_add_u64 v[124:125], v[124:125], 2, s[40:41]
	v_or_b32_e32 v122, 0x90, v132
	v_lshlrev_b32_e32 v123, 2, v122
	v_or_b32_e32 v144, v144, v122
	v_lshl_add_u64 v[128:129], v[144:145], 2, s[40:41]
	s_waitcnt vmcnt(0)
	v_pk_fma_f32 v[120:121], v[120:121], v[142:143], v[138:139]
	v_pk_fma_f32 v[118:119], v[118:119], v[140:141], v[136:137]
	global_store_dwordx4 v[124:125], v[118:121], off
	global_load_dwordx4 v[118:121], v[148:149], off offset:576 nt
	s_nop 0
	global_load_dwordx4 v[136:139], v123, s[54:55]
	v_or_b32_e32 v124, 16, v130
	v_ashrrev_i32_e32 v125, 31, v124
	v_lshlrev_b64 v[124:125], 11, v[124:125]
	v_or_b32_e32 v140, v124, v132
	v_mov_b32_e32 v141, v125
	v_lshlrev_b64 v[140:141], 2, v[140:141]
	v_lshl_add_u64 v[142:143], s[52:53], 0, v[140:141]
	s_waitcnt vmcnt(0)
	v_pk_fma_f32 v[116:117], v[116:117], v[138:139], v[120:121]
	v_pk_fma_f32 v[114:115], v[114:115], v[136:137], v[118:119]
	global_store_dwordx4 v[128:129], v[114:117], off
	global_load_dwordx4 v[114:117], v[142:143], off nt
	s_nop 0
	global_load_dwordx4 v[118:121], v133, s[54:55]
	v_lshl_add_u64 v[128:129], s[40:41], 0, v[140:141]
	s_waitcnt vmcnt(0)
	v_pk_fma_f32 v[112:113], v[112:113], v[120:121], v[116:117]
	v_pk_fma_f32 v[110:111], v[110:111], v[118:119], v[114:115]
	global_store_dwordx4 v[128:129], v[110:113], off
	global_load_dwordx4 v[110:113], v[142:143], off offset:64 nt
	s_nop 0
	global_load_dwordx4 v[114:117], v134, s[54:55]
	v_or_b32_e32 v118, v124, v131
	v_mov_b32_e32 v119, v125
	v_lshl_add_u64 v[118:119], v[118:119], 2, s[40:41]
	s_waitcnt vmcnt(0)
	v_pk_fma_f32 v[104:105], v[104:105], v[116:117], v[112:113]
	v_pk_fma_f32 v[102:103], v[102:103], v[114:115], v[110:111]
	global_store_dwordx4 v[118:119], v[102:105], off
	global_load_dwordx4 v[102:105], v[142:143], off offset:512 nt
	s_nop 0
	global_load_dwordx4 v[110:113], v127, s[54:55]
	v_or_b32_e32 v114, v124, v126
	v_mov_b32_e32 v115, v125
	v_lshl_add_u64 v[114:115], v[114:115], 2, s[40:41]
	v_or_b32_e32 v124, v124, v122
	s_waitcnt vmcnt(0)
	v_pk_fma_f32 v[104:105], v[108:109], v[112:113], v[104:105]
	v_pk_fma_f32 v[102:103], v[106:107], v[110:111], v[102:103]
	global_store_dwordx4 v[114:115], v[102:105], off
	global_load_dwordx4 v[102:105], v[142:143], off offset:576 nt
	s_nop 0
	global_load_dwordx4 v[106:109], v123, s[54:55]
	v_or_b32_e32 v110, 32, v130
	v_ashrrev_i32_e32 v111, 31, v110
	v_lshlrev_b64 v[110:111], 11, v[110:111]
	v_or_b32_e32 v112, v110, v132
	v_mov_b32_e32 v113, v111
	v_lshl_add_u64 v[114:115], v[124:125], 2, s[40:41]
	v_lshlrev_b64 v[112:113], 2, v[112:113]
	v_lshl_add_u64 v[116:117], s[52:53], 0, v[112:113]
	s_waitcnt vmcnt(0)
	v_pk_fma_f32 v[100:101], v[100:101], v[108:109], v[104:105]
	v_pk_fma_f32 v[98:99], v[98:99], v[106:107], v[102:103]
	global_store_dwordx4 v[114:115], v[98:101], off
	global_load_dwordx4 v[98:101], v[116:117], off nt
	s_nop 0
	global_load_dwordx4 v[102:105], v133, s[54:55]
	v_lshl_add_u64 v[106:107], s[40:41], 0, v[112:113]
	s_waitcnt vmcnt(0)
	v_pk_fma_f32 v[96:97], v[96:97], v[104:105], v[100:101]
	v_pk_fma_f32 v[94:95], v[94:95], v[102:103], v[98:99]
	global_store_dwordx4 v[106:107], v[94:97], off
	global_load_dwordx4 v[94:97], v[116:117], off offset:64 nt
	s_nop 0
	global_load_dwordx4 v[98:101], v134, s[54:55]
	v_or_b32_e32 v102, v110, v131
	v_mov_b32_e32 v103, v111
	v_lshl_add_u64 v[102:103], v[102:103], 2, s[40:41]
	s_waitcnt vmcnt(0)
	v_pk_fma_f32 v[88:89], v[88:89], v[100:101], v[96:97]
	v_pk_fma_f32 v[86:87], v[86:87], v[98:99], v[94:95]
	global_store_dwordx4 v[102:103], v[86:89], off
	global_load_dwordx4 v[86:89], v[116:117], off offset:512 nt
	s_nop 0
	global_load_dwordx4 v[94:97], v127, s[54:55]
	v_or_b32_e32 v98, v110, v126
	v_mov_b32_e32 v99, v111
	v_lshl_add_u64 v[98:99], v[98:99], 2, s[40:41]
	v_or_b32_e32 v110, v110, v122
	s_waitcnt vmcnt(0)
; __device__ __forceinline__ void phase_out(const Ptrs& p, LAS unsigned char* lds) {
;     ...
;         for (int ai = 0; ai < 2; ++ai)
; #pragma unroll
;             for (int m = 0; m < 4; ++m) { const int row = row0 + ai * 128 + wr * 64 + m * 16 + fr;
; #pragma unroll
;                 for (int bj = 0; bj < 2; ++bj)
; #pragma unroll
;                     for (int n = 0; n < 2; ++n) { const int c = col0 + bj * 128 + wc * 32 + n * 16 + fq * 4; const size_t o = (size_t)row * D + c;
;                         *(f32x4*)(x1 + o) = *(const f32x4*)(p.x + o) + *(const f32x4*)(gm + c) * acc[ai][bj][m][n]; } }
	v_pk_fma_f32 v[88:89], v[92:93], v[96:97], v[88:89]
	v_pk_fma_f32 v[86:87], v[90:91], v[94:95], v[86:87]
	global_store_dwordx4 v[98:99], v[86:89], off
	global_load_dwordx4 v[86:89], v[116:117], off offset:576 nt
	s_nop 0
	global_load_dwordx4 v[90:93], v123, s[54:55]
	v_or_b32_e32 v94, 48, v130
	v_ashrrev_i32_e32 v95, 31, v94
	v_lshlrev_b64 v[94:95], 11, v[94:95]
	v_or_b32_e32 v96, v94, v132
	v_mov_b32_e32 v97, v95
	v_lshl_add_u64 v[98:99], v[110:111], 2, s[40:41]
	v_lshlrev_b64 v[96:97], 2, v[96:97]
	v_lshl_add_u64 v[100:101], s[52:53], 0, v[96:97]
	s_waitcnt vmcnt(0)
	v_pk_fma_f32 v[84:85], v[84:85], v[92:93], v[88:89]
	v_pk_fma_f32 v[82:83], v[82:83], v[90:91], v[86:87]
	global_store_dwordx4 v[98:99], v[82:85], off
	global_load_dwordx4 v[82:85], v[100:101], off nt
	s_nop 0
	global_load_dwordx4 v[86:89], v133, s[54:55]
	v_lshl_add_u64 v[90:91], s[40:41], 0, v[96:97]
	s_waitcnt vmcnt(0)
	v_pk_fma_f32 v[80:81], v[80:81], v[88:89], v[84:85]
	v_pk_fma_f32 v[78:79], v[78:79], v[86:87], v[82:83]
	global_store_dwordx4 v[90:91], v[78:81], off
	global_load_dwordx4 v[78:81], v[100:101], off offset:64 nt
	s_nop 0
	global_load_dwordx4 v[82:85], v134, s[54:55]
	v_or_b32_e32 v86, v94, v131
	v_mov_b32_e32 v87, v95
	v_lshl_add_u64 v[86:87], v[86:87], 2, s[40:41]
	s_waitcnt vmcnt(0)
	v_pk_fma_f32 v[72:73], v[72:73], v[84:85], v[80:81]
	v_pk_fma_f32 v[70:71], v[70:71], v[82:83], v[78:79]
	global_store_dwordx4 v[86:87], v[70:73], off
	global_load_dwordx4 v[70:73], v[100:101], off offset:512 nt
	s_nop 0
	global_load_dwordx4 v[78:81], v127, s[54:55]
	v_or_b32_e32 v82, v94, v126
	v_mov_b32_e32 v83, v95
	v_lshl_add_u64 v[82:83], v[82:83], 2, s[40:41]
	v_or_b32_e32 v94, v94, v122
	s_waitcnt vmcnt(0)
	v_pk_fma_f32 v[72:73], v[76:77], v[80:81], v[72:73]
	v_pk_fma_f32 v[70:71], v[74:75], v[78:79], v[70:71]
	global_store_dwordx4 v[82:83], v[70:73], off
	global_load_dwordx4 v[70:73], v[100:101], off offset:576 nt
	s_nop 0
	global_load_dwordx4 v[74:77], v123, s[54:55]
	v_add_u32_e32 v78, 0x80, v130
	v_ashrrev_i32_e32 v79, 31, v78
	v_lshlrev_b64 v[78:79], 11, v[78:79]
	v_or_b32_e32 v80, v78, v132
	v_mov_b32_e32 v81, v79
	v_lshl_add_u64 v[82:83], v[94:95], 2, s[40:41]
	v_lshlrev_b64 v[80:81], 2, v[80:81]
	v_lshl_add_u64 v[84:85], s[52:53], 0, v[80:81]
	s_waitcnt vmcnt(0)
	v_pk_fma_f32 v[64:65], v[64:65], v[76:77], v[72:73]
	v_pk_fma_f32 v[62:63], v[62:63], v[74:75], v[70:71]
	global_store_dwordx4 v[82:83], v[62:65], off
	global_load_dwordx4 v[62:65], v[84:85], off nt
	s_nop 0
	global_load_dwordx4 v[70:73], v133, s[54:55]
	v_lshl_add_u64 v[74:75], s[40:41], 0, v[80:81]
	s_waitcnt vmcnt(0)
	v_pk_fma_f32 v[64:65], v[68:69], v[72:73], v[64:65]
	v_pk_fma_f32 v[62:63], v[66:67], v[70:71], v[62:63]
	global_store_dwordx4 v[74:75], v[62:65], off
	global_load_dwordx4 v[62:65], v[84:85], off offset:64 nt
	s_nop 0
	global_load_dwordx4 v[66:69], v134, s[54:55]
	v_or_b32_e32 v70, v78, v131
	v_mov_b32_e32 v71, v79
	v_lshl_add_u64 v[70:71], v[70:71], 2, s[40:41]
	s_waitcnt vmcnt(0)
	v_pk_fma_f32 v[60:61], v[60:61], v[68:69], v[64:65]
	v_pk_fma_f32 v[58:59], v[58:59], v[66:67], v[62:63]
	global_store_dwordx4 v[70:71], v[58:61], off
	global_load_dwordx4 v[58:61], v[84:85], off offset:512 nt
	s_nop 0
	global_load_dwordx4 v[62:65], v127, s[54:55]
	v_or_b32_e32 v66, v78, v126
	v_mov_b32_e32 v67, v79
	v_lshl_add_u64 v[66:67], v[66:67], 2, s[40:41]
	v_or_b32_e32 v78, v78, v122
	s_waitcnt vmcnt(0)
	v_pk_fma_f32 v[56:57], v[56:57], v[64:65], v[60:61]
	v_pk_fma_f32 v[54:55], v[54:55], v[62:63], v[58:59]
	global_store_dwordx4 v[66:67], v[54:57], off
	global_load_dwordx4 v[54:57], v[84:85], off offset:576 nt
	s_nop 0
	global_load_dwordx4 v[58:61], v123, s[54:55]
	v_add_u32_e32 v62, 0x90, v130
	v_ashrrev_i32_e32 v63, 31, v62
	v_lshlrev_b64 v[62:63], 11, v[62:63]
	v_or_b32_e32 v64, v62, v132
	v_mov_b32_e32 v65, v63
	v_lshl_add_u64 v[66:67], v[78:79], 2, s[40:41]
	v_lshlrev_b64 v[64:65], 2, v[64:65]
	v_lshl_add_u64 v[68:69], s[52:53], 0, v[64:65]
	s_waitcnt vmcnt(0)
	v_pk_fma_f32 v[52:53], v[52:53], v[60:61], v[56:57]
	v_pk_fma_f32 v[50:51], v[50:51], v[58:59], v[54:55]
	global_store_dwordx4 v[66:67], v[50:53], off
	global_load_dwordx4 v[50:53], v[68:69], off nt
	s_nop 0
	global_load_dwordx4 v[54:57], v133, s[54:55]
	v_lshl_add_u64 v[58:59], s[40:41], 0, v[64:65]
	s_waitcnt vmcnt(0)
; __device__ __forceinline__ void phase_out(const Ptrs& p, LAS unsigned char* lds) {
;     ...
;         for (int ai = 0; ai < 2; ++ai)
; #pragma unroll
;             for (int m = 0; m < 4; ++m) { const int row = row0 + ai * 128 + wr * 64 + m * 16 + fr;
; #pragma unroll
;                 for (int bj = 0; bj < 2; ++bj)
; #pragma unroll
;                     for (int n = 0; n < 2; ++n) { const int c = col0 + bj * 128 + wc * 32 + n * 16 + fq * 4; const size_t o = (size_t)row * D + c;
;                         *(f32x4*)(x1 + o) = *(const f32x4*)(p.x + o) + *(const f32x4*)(gm + c) * acc[ai][bj][m][n]; } }
;     }
	v_pk_fma_f32 v[48:49], v[48:49], v[56:57], v[52:53]
	v_pk_fma_f32 v[46:47], v[46:47], v[54:55], v[50:51]
	global_store_dwordx4 v[58:59], v[46:49], off
	global_load_dwordx4 v[46:49], v[68:69], off offset:64 nt
	s_nop 0
	global_load_dwordx4 v[50:53], v134, s[54:55]
	v_or_b32_e32 v54, v62, v131
	v_mov_b32_e32 v55, v63
	v_lshl_add_u64 v[54:55], v[54:55], 2, s[40:41]
	s_waitcnt vmcnt(0)
	v_pk_fma_f32 v[44:45], v[44:45], v[52:53], v[48:49]
	v_pk_fma_f32 v[42:43], v[42:43], v[50:51], v[46:47]
	global_store_dwordx4 v[54:55], v[42:45], off
	global_load_dwordx4 v[42:45], v[68:69], off offset:512 nt
	s_nop 0
	global_load_dwordx4 v[46:49], v127, s[54:55]
	v_or_b32_e32 v50, v62, v126
	v_mov_b32_e32 v51, v63
	v_lshl_add_u64 v[50:51], v[50:51], 2, s[40:41]
	v_or_b32_e32 v62, v62, v122
	s_waitcnt vmcnt(0)
	v_pk_fma_f32 v[40:41], v[40:41], v[48:49], v[44:45]
	v_pk_fma_f32 v[38:39], v[38:39], v[46:47], v[42:43]
	global_store_dwordx4 v[50:51], v[38:41], off
	global_load_dwordx4 v[38:41], v[68:69], off offset:576 nt
	s_nop 0
	global_load_dwordx4 v[42:45], v123, s[54:55]
	v_add_u32_e32 v46, 0xa0, v130
	v_ashrrev_i32_e32 v47, 31, v46
	v_lshlrev_b64 v[46:47], 11, v[46:47]
	v_or_b32_e32 v48, v46, v132
	v_mov_b32_e32 v49, v47
	v_lshl_add_u64 v[50:51], v[62:63], 2, s[40:41]
	v_lshlrev_b64 v[48:49], 2, v[48:49]
	v_lshl_add_u64 v[52:53], s[52:53], 0, v[48:49]
	s_waitcnt vmcnt(0)
	v_pk_fma_f32 v[36:37], v[36:37], v[44:45], v[40:41]
	v_pk_fma_f32 v[34:35], v[34:35], v[42:43], v[38:39]
	global_store_dwordx4 v[50:51], v[34:37], off
	global_load_dwordx4 v[34:37], v[52:53], off nt
	s_nop 0
	global_load_dwordx4 v[38:41], v133, s[54:55]
	v_lshl_add_u64 v[42:43], s[40:41], 0, v[48:49]
	s_waitcnt vmcnt(0)
	v_pk_fma_f32 v[32:33], v[32:33], v[40:41], v[36:37]
	v_pk_fma_f32 v[30:31], v[30:31], v[38:39], v[34:35]
	global_store_dwordx4 v[42:43], v[30:33], off
	global_load_dwordx4 v[30:33], v[52:53], off offset:64 nt
	s_nop 0
	global_load_dwordx4 v[34:37], v134, s[54:55]
	v_or_b32_e32 v38, v46, v131
	v_mov_b32_e32 v39, v47
	v_lshl_add_u64 v[38:39], v[38:39], 2, s[40:41]
	s_waitcnt vmcnt(0)
	v_pk_fma_f32 v[28:29], v[28:29], v[36:37], v[32:33]
	v_pk_fma_f32 v[26:27], v[26:27], v[34:35], v[30:31]
	global_store_dwordx4 v[38:39], v[26:29], off
	global_load_dwordx4 v[26:29], v[52:53], off offset:512 nt
	s_nop 0
	global_load_dwordx4 v[30:33], v127, s[54:55]
	v_or_b32_e32 v34, v46, v126
	v_mov_b32_e32 v35, v47
	v_lshl_add_u64 v[34:35], v[34:35], 2, s[40:41]
	v_or_b32_e32 v46, v46, v122
	s_waitcnt vmcnt(0)
	v_pk_fma_f32 v[24:25], v[24:25], v[32:33], v[28:29]
	v_pk_fma_f32 v[22:23], v[22:23], v[30:31], v[26:27]
	global_store_dwordx4 v[34:35], v[22:25], off
	global_load_dwordx4 v[22:25], v[52:53], off offset:576 nt
	s_nop 0
	global_load_dwordx4 v[26:29], v123, s[54:55]
	v_add_u32_e32 v30, 0xb0, v130
	v_ashrrev_i32_e32 v31, 31, v30
	v_lshlrev_b64 v[30:31], 11, v[30:31]
	v_or_b32_e32 v32, v30, v132
	v_mov_b32_e32 v33, v31
	v_lshl_add_u64 v[34:35], v[46:47], 2, s[40:41]
	v_lshlrev_b64 v[32:33], 2, v[32:33]
	v_lshl_add_u64 v[36:37], s[52:53], 0, v[32:33]
	s_waitcnt vmcnt(0)
	v_pk_fma_f32 v[20:21], v[20:21], v[28:29], v[24:25]
	v_pk_fma_f32 v[18:19], v[18:19], v[26:27], v[22:23]
	global_store_dwordx4 v[34:35], v[18:21], off
	global_load_dwordx4 v[18:21], v[36:37], off nt
	s_nop 0
	global_load_dwordx4 v[22:25], v133, s[54:55]
	v_lshl_add_u64 v[26:27], s[40:41], 0, v[32:33]
	s_waitcnt vmcnt(0)
	v_pk_fma_f32 v[16:17], v[16:17], v[24:25], v[20:21]
	v_pk_fma_f32 v[14:15], v[14:15], v[22:23], v[18:19]
	global_store_dwordx4 v[26:27], v[14:17], off
	global_load_dwordx4 v[14:17], v[36:37], off offset:64 nt
	s_nop 0
	global_load_dwordx4 v[18:21], v134, s[54:55]
	v_or_b32_e32 v22, v30, v131
	v_mov_b32_e32 v23, v31
	v_lshl_add_u64 v[22:23], v[22:23], 2, s[40:41]
	s_waitcnt vmcnt(0)
	v_pk_fma_f32 v[12:13], v[12:13], v[20:21], v[16:17]
	v_pk_fma_f32 v[10:11], v[10:11], v[18:19], v[14:15]
	global_store_dwordx4 v[22:23], v[10:13], off
	global_load_dwordx4 v[10:13], v[36:37], off offset:512 nt
	s_nop 0
	global_load_dwordx4 v[14:17], v127, s[54:55]
	v_or_b32_e32 v18, v30, v126
	v_mov_b32_e32 v19, v31
	v_lshl_add_u64 v[18:19], v[18:19], 2, s[40:41]
	v_or_b32_e32 v30, v30, v122
	s_waitcnt vmcnt(0)
	v_pk_fma_f32 v[8:9], v[8:9], v[16:17], v[12:13]
	v_pk_fma_f32 v[6:7], v[6:7], v[14:15], v[10:11]
	global_store_dwordx4 v[18:19], v[6:9], off
	global_load_dwordx4 v[6:9], v[36:37], off offset:576 nt
	s_nop 0
	global_load_dwordx4 v[10:13], v123, s[54:55]
	v_lshl_add_u64 v[14:15], v[30:31], 2, s[40:41]
	s_waitcnt vmcnt(0)
	v_pk_fma_f32 v[4:5], v[4:5], v[12:13], v[8:9]
	v_pk_fma_f32 v[2:3], v[2:3], v[10:11], v[6:7]
	global_store_dwordx4 v[14:15], v[2:5], off
	s_cbranch_vccz .LBB0_851
